# speedup vs baseline: 1.0034x; 1.0034x over previous
.Lp_main:
	s_load_dwordx2 s[10:11], s[0:1], 0x0
	s_load_dwordx4 s[12:15], s[0:1], 0x10
	s_load_dwordx2 s[16:17], s[0:1], 0x20
	s_load_dwordx4 s[20:23], s[0:1], 0x28
	v_readfirstlane_b32 s3, v0
	v_and_b32_e32 v154, 63, v0
	v_lshrrev_b32_e32 v155, 5, v154
	v_lshlrev_b32_e32 v156, 4, v0
	v_lshlrev_b32_e32 v157, 4, v154
	v_lshlrev_b32_e32 v158, 8, v1
	v_lshl_add_u32 v158, v155, 5, v158
	v_lshlrev_b32_e32 v159, 4, v155
	v_lshrrev_b32_e32 v160, 3, v0
	v_lshlrev_b32_e32 v160, 12, v160
	v_and_b32_e32 v161, 7, v0
	v_lshl_add_u32 v160, v161, 4, v160
	s_lshr_b32 s41, s2, 3
	s_and_b32 s42, s2, 7
	s_lshl_b32 s24, s42, 2
	s_bfe_u32 s25, s2, 0x20003
	s_add_u32 s24, s24, s25
	s_lshr_b32 s25, s2, 5
	s_lshr_b32 s26, s3, 6
	s_lshl_b32 s27, s25, 2
	s_add_u32 s27, s27, s26
	s_mov_b32 s4, 0x4038aa3b
	s_mov_b32 s5, s4
	s_lshl_b32 s40, s26, 6
	s_waitcnt lgkmcnt(0)
	s_lshl_b32 s28, s24, 15
	s_add_u32 s28, s28, 0x1000
	s_add_u32 s10, s10, s28
	s_addc_u32 s11, s11, 0
	s_lshl_b32 s34, s41, 17
	s_lshl_b32 s35, s42, 9
	s_add_u32 s34, s34, s35
	s_add_u32 s34, s14, s34
	s_addc_u32 s35, s15, 0
	s_lshl_b32 s28, s27, 13
	s_add_u32 s28, s8, s28
	s_addc_u32 s29, s9, 0
	s_lshl_b32 s30, s27, 7
	s_add_u32 s30, s12, s30
	s_addc_u32 s31, s13, 0
	global_load_dwordx4 v[2:5], v156, s[10:11] offset:-4096
	global_load_dwordx4 v[6:9], v156, s[10:11] offset:0
	s_add_u32 s10, s10, 0x2000
	s_addc_u32 s11, s11, 0
	global_load_dwordx4 v[10:13], v156, s[10:11] offset:-4096
	global_load_dwordx4 v[14:17], v156, s[10:11] offset:0
	s_add_u32 s10, s10, 0x2000
	s_addc_u32 s11, s11, 0
	global_load_dwordx4 v[18:21], v156, s[10:11] offset:-4096
	global_load_dwordx4 v[22:25], v156, s[10:11] offset:0
	s_add_u32 s10, s10, 0x2000
	s_addc_u32 s11, s11, 0
	global_load_dwordx4 v[26:29], v156, s[10:11] offset:-4096
	global_load_dwordx4 v[30:33], v156, s[10:11] offset:0
	global_load_dwordx4 v[130:133], v160, s[34:35] offset:0
	global_load_dwordx4 v[134:137], v160, s[34:35] offset:128
	global_load_dwordx4 v[138:141], v160, s[34:35] offset:256
	global_load_dwordx4 v[142:145], v160, s[34:35] offset:384
	global_load_dwordx4 v[34:37], v158, s[28:29] offset:0
	global_load_dwordx4 v[38:41], v158, s[28:29] offset:16
	global_load_dwordx4 v[42:45], v158, s[28:29] offset:64
	global_load_dwordx4 v[46:49], v158, s[28:29] offset:80
	global_load_dwordx4 v[50:53], v158, s[28:29] offset:128
	global_load_dwordx4 v[54:57], v158, s[28:29] offset:144
	global_load_dwordx4 v[58:61], v158, s[28:29] offset:192
	global_load_dwordx4 v[62:65], v158, s[28:29] offset:208
	s_load_dwordx16 s[48:63], s[30:31], 0x0
	s_load_dwordx16 s[64:79], s[30:31], 0x40
	v_bfe_u32 v163, v0, 1, 3
	v_mul_u32_u24_e32 v163, 0x210, v163
	v_lshrrev_b32_e32 v164, 4, v0
	v_lshl_add_u32 v163, v164, 4, v163
	v_and_b32_e32 v164, 1, v0
	v_lshl_add_u32 v163, v164, 3, v163
	v_lshrrev_b32_e32 v164, 3, v0
	v_mul_u32_u24_e32 v164, 0x110, v164
	v_lshl_add_u32 v164, v161, 3, v164
	v_add_u32_e32 v164, 0x4200, v164
	v_mul_u32_u24_e32 v165, 0x210, v155
	v_lshl_add_u32 v165, v1, 4, v165
	v_mul_u32_u24_e32 v166, 0x110, v1
	v_lshl_add_u32 v166, v155, 4, v166
	v_add_u32_e32 v166, s40, v166
	v_add_u32_e32 v166, 0x4200, v166
	v_mul_u32_u24_e32 v167, 0x880, v155
	v_lshl_add_u32 v167, v1, 1, v167
	v_add_u32_e32 v167, s40, v167
	v_add_u32_e32 v167, 0x4200, v167
	s_lshl_b32 s32, s24, 18
	s_lshl_b32 s33, s27, 11
	s_add_u32 s32, s32, s33
	s_add_u32 s32, s16, s32
	s_addc_u32 s33, s17, 0
	s_lshl_b32 s36, s41, 16
	s_lshl_b32 s37, s42, 13
	s_add_u32 s36, s36, s37
	s_lshl_b32 s37, s26, 11
	s_add_u32 s36, s36, s37
	s_add_u32 s36, s20, s36
	s_addc_u32 s37, s21, 0
	s_lshl_b32 s38, s42, 18
	s_lshl_b32 s39, s26, 16
	s_add_u32 s38, s38, s39
	s_lshl_b32 s39, s41, 11
	s_add_u32 s38, s38, s39
	s_add_u32 s38, s22, s38
	s_addc_u32 s39, s23, 0
	s_waitcnt vmcnt(19)
	v_cvt_pk_f16_f32 v2, v2, v3
	v_cvt_pk_f16_f32 v3, v4, v5
	ds_write_b64 v163, v[2:3] offset:0
	s_waitcnt vmcnt(18)
	v_cvt_pk_f16_f32 v6, v6, v7
	v_cvt_pk_f16_f32 v7, v8, v9
	ds_write_b64 v163, v[6:7] offset:256
	s_waitcnt vmcnt(17)
	v_cvt_pk_f16_f32 v10, v10, v11
	v_cvt_pk_f16_f32 v11, v12, v13
	ds_write_b64 v163, v[10:11] offset:4224
	s_waitcnt vmcnt(16)
	v_cvt_pk_f16_f32 v14, v14, v15
	v_cvt_pk_f16_f32 v15, v16, v17
	ds_write_b64 v163, v[14:15] offset:4480
	s_waitcnt vmcnt(15)
	v_cvt_pk_f16_f32 v18, v18, v19
	v_cvt_pk_f16_f32 v19, v20, v21
	ds_write_b64 v163, v[18:19] offset:8448
	s_waitcnt vmcnt(14)
	v_cvt_pk_f16_f32 v22, v22, v23
	v_cvt_pk_f16_f32 v23, v24, v25
	ds_write_b64 v163, v[22:23] offset:8704
	s_waitcnt vmcnt(13)
	v_cvt_pk_f16_f32 v26, v26, v27
	v_cvt_pk_f16_f32 v27, v28, v29
	ds_write_b64 v163, v[26:27] offset:12672
	s_waitcnt vmcnt(12)
	v_cvt_pk_f16_f32 v30, v30, v31
	v_cvt_pk_f16_f32 v31, v32, v33
	ds_write_b64 v163, v[30:31] offset:12928
	s_waitcnt vmcnt(11)
	v_cvt_pk_f16_f32 v130, v130, v131
	v_cvt_pk_f16_f32 v131, v132, v133
	ds_write_b64 v164, v[130:131] offset:0
	s_waitcnt vmcnt(10)
	v_cvt_pk_f16_f32 v134, v134, v135
	v_cvt_pk_f16_f32 v135, v136, v137
	ds_write_b64 v164, v[134:135] offset:64
	s_waitcnt vmcnt(9)
	v_cvt_pk_f16_f32 v138, v138, v139
	v_cvt_pk_f16_f32 v139, v140, v141
	ds_write_b64 v164, v[138:139] offset:128
	s_waitcnt vmcnt(8)
	v_cvt_pk_f16_f32 v142, v142, v143
	v_cvt_pk_f16_f32 v143, v144, v145
	ds_write_b64 v164, v[142:143] offset:192
	s_waitcnt lgkmcnt(0)
	s_barrier
	ds_read_b128 v[130:133], v166
	ds_read_b128 v[134:137], v166 offset:32
	ds_read_u16 v138, v167 offset:0
	ds_read_u16 v139, v167 offset:272
	ds_read_u16 v140, v167 offset:544
	ds_read_u16 v141, v167 offset:816
	ds_read_u16 v142, v167 offset:1088
	ds_read_u16 v143, v167 offset:1360
	ds_read_u16 v144, v167 offset:1632
	ds_read_u16 v145, v167 offset:1904
	s_waitcnt vmcnt(0)
	v_cvt_pk_f16_f32 v82, v34, v35
	v_cvt_pk_f16_f32 v83, v36, v37
	v_cvt_pk_f16_f32 v84, v38, v39
	v_cvt_pk_f16_f32 v85, v40, v41
	v_cvt_pk_f16_f32 v86, v42, v43
	v_cvt_pk_f16_f32 v87, v44, v45
	v_cvt_pk_f16_f32 v88, v46, v47
	v_cvt_pk_f16_f32 v89, v48, v49
	v_cvt_pk_f16_f32 v90, v50, v51
	v_cvt_pk_f16_f32 v91, v52, v53
	v_cvt_pk_f16_f32 v92, v54, v55
	v_cvt_pk_f16_f32 v93, v56, v57
	v_cvt_pk_f16_f32 v94, v58, v59
	v_cvt_pk_f16_f32 v95, v60, v61
	v_cvt_pk_f16_f32 v96, v62, v63
	v_cvt_pk_f16_f32 v97, v64, v65
	v_cmp_lt_u32_e32 vcc, 31, v154
	v_mov_b32_e32 v66, s48
	v_mov_b32_e32 v162, s52
	v_cndmask_b32_e32 v66, v66, v162, vcc
	v_mov_b32_e32 v67, s49
	v_mov_b32_e32 v162, s53
	v_cndmask_b32_e32 v67, v67, v162, vcc
	v_mov_b32_e32 v68, s50
	v_mov_b32_e32 v162, s54
	v_cndmask_b32_e32 v68, v68, v162, vcc
	v_mov_b32_e32 v69, s51
	v_mov_b32_e32 v162, s55
	v_cndmask_b32_e32 v69, v69, v162, vcc
	v_mov_b32_e32 v70, s56
	v_mov_b32_e32 v162, s60
	v_cndmask_b32_e32 v70, v70, v162, vcc
	v_mov_b32_e32 v71, s57
	v_mov_b32_e32 v162, s61
	v_cndmask_b32_e32 v71, v71, v162, vcc
	v_mov_b32_e32 v72, s58
	v_mov_b32_e32 v162, s62
	v_cndmask_b32_e32 v72, v72, v162, vcc
	v_mov_b32_e32 v73, s59
	v_mov_b32_e32 v162, s63
	v_cndmask_b32_e32 v73, v73, v162, vcc
	v_mov_b32_e32 v74, s64
	v_mov_b32_e32 v162, s68
	v_cndmask_b32_e32 v74, v74, v162, vcc
	v_mov_b32_e32 v75, s65
	v_mov_b32_e32 v162, s69
	v_cndmask_b32_e32 v75, v75, v162, vcc
	v_mov_b32_e32 v76, s66
	v_mov_b32_e32 v162, s70
	v_cndmask_b32_e32 v76, v76, v162, vcc
	v_mov_b32_e32 v77, s67
	v_mov_b32_e32 v162, s71
	v_cndmask_b32_e32 v77, v77, v162, vcc
	v_mov_b32_e32 v78, s72
	v_mov_b32_e32 v162, s76
	v_cndmask_b32_e32 v78, v78, v162, vcc
	v_mov_b32_e32 v79, s73
	v_mov_b32_e32 v162, s77
	v_cndmask_b32_e32 v79, v79, v162, vcc
	v_mov_b32_e32 v80, s74
	v_mov_b32_e32 v162, s78
	v_cndmask_b32_e32 v80, v80, v162, vcc
	v_mov_b32_e32 v81, s75
	v_mov_b32_e32 v162, s79
	v_cndmask_b32_e32 v81, v81, v162, vcc
	v_pk_mul_f32 v[66:67], v[66:67], s[4:5] op_sel_hi:[1,0]
	v_pk_mul_f32 v[68:69], v[68:69], s[4:5] op_sel_hi:[1,0]
	v_pk_mul_f32 v[70:71], v[70:71], s[4:5] op_sel_hi:[1,0]
	v_pk_mul_f32 v[72:73], v[72:73], s[4:5] op_sel_hi:[1,0]
	v_pk_mul_f32 v[74:75], v[74:75], s[4:5] op_sel_hi:[1,0]
	v_pk_mul_f32 v[76:77], v[76:77], s[4:5] op_sel_hi:[1,0]
	v_pk_mul_f32 v[78:79], v[78:79], s[4:5] op_sel_hi:[1,0]
	v_pk_mul_f32 v[80:81], v[80:81], s[4:5] op_sel_hi:[1,0]
	s_waitcnt lgkmcnt(8)
	global_store_dwordx4 v157, v[130:133], s[36:37] sc1
	global_store_dwordx4 v157, v[134:137], s[36:37] offset:1024 sc1
	s_waitcnt lgkmcnt(0)
	v_lshl_or_b32 v138, v139, 16, v138
	v_lshl_or_b32 v139, v141, 16, v140
	v_lshl_or_b32 v140, v143, 16, v142
	v_lshl_or_b32 v141, v145, 16, v144
	global_store_dwordx4 v157, v[138:141], s[38:39] sc1
	ds_read_u16 v142, v167 offset:4352
	ds_read_u16 v143, v167 offset:4624
	ds_read_u16 v144, v167 offset:4896
	ds_read_u16 v145, v167 offset:5168
	ds_read_u16 v146, v167 offset:5440
	ds_read_u16 v147, v167 offset:5712
	ds_read_u16 v148, v167 offset:5984
	ds_read_u16 v149, v167 offset:6256
	ds_read_b128 v[2:5], v165 offset:0
	ds_read_b128 v[6:9], v165 offset:1056
	ds_read_b128 v[10:13], v165 offset:2112
	ds_read_b128 v[14:17], v165 offset:3168
	s_waitcnt lgkmcnt(4)
	v_lshl_or_b32 v142, v143, 16, v142
	v_lshl_or_b32 v143, v145, 16, v144
	v_lshl_or_b32 v144, v147, 16, v146
	v_lshl_or_b32 v145, v149, 16, v148
	global_store_dwordx4 v157, v[142:145], s[38:39] offset:1024 sc1
	ds_read_b128 v[18:21], v165 offset:4224
	ds_read_b128 v[22:25], v165 offset:5280
	ds_read_b128 v[26:29], v165 offset:6336
	ds_read_b128 v[30:33], v165 offset:7392
	ds_read_b128 v[34:37], v165 offset:8448
	ds_read_b128 v[38:41], v165 offset:9504
	ds_read_b128 v[42:45], v165 offset:10560
	ds_read_b128 v[46:49], v165 offset:11616
	s_waitcnt lgkmcnt(8)
	v_mfma_f32_32x32x16_f16 v[98:113], v[82:85], v[2:5], 0
	v_mfma_f32_32x32x16_f16 v[98:113], v[86:89], v[6:9], v[98:113]
	v_mfma_f32_32x32x16_f16 v[98:113], v[90:93], v[10:13], v[98:113]
	v_mfma_f32_32x32x16_f16 v[98:113], v[94:97], v[14:17], v[98:113]
	ds_read_b128 v[50:53], v165 offset:12672
	ds_read_b128 v[54:57], v165 offset:13728
	ds_read_b128 v[58:61], v165 offset:14784
	ds_read_b128 v[62:65], v165 offset:15840
	s_waitcnt lgkmcnt(8)
	v_mfma_f32_32x32x16_f16 v[114:129], v[82:85], v[18:21], 0
	v_mfma_f32_32x32x16_f16 v[114:129], v[86:89], v[22:25], v[114:129]
	v_mfma_f32_32x32x16_f16 v[114:129], v[90:93], v[26:29], v[114:129]
	v_mfma_f32_32x32x16_f16 v[114:129], v[94:97], v[30:33], v[114:129]
	s_nop 7
	v_pk_fma_f32 v[130:131], v[98:99], s[4:5], v[66:67] op_sel_hi:[1,0,1]
	v_pk_fma_f32 v[132:133], v[100:101], s[4:5], v[68:69] op_sel_hi:[1,0,1]
	v_pk_fma_f32 v[134:135], v[102:103], s[4:5], v[70:71] op_sel_hi:[1,0,1]
	v_pk_fma_f32 v[136:137], v[104:105], s[4:5], v[72:73] op_sel_hi:[1,0,1]
	v_pk_fma_f32 v[138:139], v[106:107], s[4:5], v[74:75] op_sel_hi:[1,0,1]
	v_pk_fma_f32 v[140:141], v[108:109], s[4:5], v[76:77] op_sel_hi:[1,0,1]
	v_pk_fma_f32 v[142:143], v[110:111], s[4:5], v[78:79] op_sel_hi:[1,0,1]
	v_pk_fma_f32 v[144:145], v[112:113], s[4:5], v[80:81] op_sel_hi:[1,0,1]
	v_exp_f32_e32 v130, v130
	v_exp_f32_e32 v131, v131
	v_exp_f32_e32 v132, v132
	v_exp_f32_e32 v133, v133
	v_exp_f32_e32 v134, v134
	v_exp_f32_e32 v135, v135
	v_exp_f32_e32 v136, v136
	v_exp_f32_e32 v137, v137
	v_exp_f32_e32 v138, v138
	v_exp_f32_e32 v139, v139
	v_exp_f32_e32 v140, v140
	v_exp_f32_e32 v141, v141
	v_exp_f32_e32 v142, v142
	v_exp_f32_e32 v143, v143
	v_exp_f32_e32 v144, v144
	v_exp_f32_e32 v145, v145
	v_pk_add_f32 v[130:131], v[130:131], 1.0 op_sel_hi:[1,0]
	v_pk_add_f32 v[132:133], v[132:133], 1.0 op_sel_hi:[1,0]
	v_pk_add_f32 v[134:135], v[134:135], 1.0 op_sel_hi:[1,0]
	v_pk_add_f32 v[136:137], v[136:137], 1.0 op_sel_hi:[1,0]
	v_pk_add_f32 v[138:139], v[138:139], 1.0 op_sel_hi:[1,0]
	v_pk_add_f32 v[140:141], v[140:141], 1.0 op_sel_hi:[1,0]
	v_pk_add_f32 v[142:143], v[142:143], 1.0 op_sel_hi:[1,0]
	v_pk_add_f32 v[144:145], v[144:145], 1.0 op_sel_hi:[1,0]
	v_rcp_f32_e32 v130, v130
	v_rcp_f32_e32 v131, v131
	v_rcp_f32_e32 v132, v132
	v_rcp_f32_e32 v133, v133
	v_rcp_f32_e32 v134, v134
	v_rcp_f32_e32 v135, v135
	v_rcp_f32_e32 v136, v136
	v_rcp_f32_e32 v137, v137
	v_rcp_f32_e32 v138, v138
	v_rcp_f32_e32 v139, v139
	v_rcp_f32_e32 v140, v140
	v_rcp_f32_e32 v141, v141
	v_rcp_f32_e32 v142, v142
	v_rcp_f32_e32 v143, v143
	v_rcp_f32_e32 v144, v144
	v_rcp_f32_e32 v145, v145
	v_pk_fma_f32 v[130:131], v[130:131], 2.0, 1.0 op_sel_hi:[1,0,0] neg_lo:[1,0,0] neg_hi:[1,0,0]
	v_pk_fma_f32 v[132:133], v[132:133], 2.0, 1.0 op_sel_hi:[1,0,0] neg_lo:[1,0,0] neg_hi:[1,0,0]
	v_pk_fma_f32 v[134:135], v[134:135], 2.0, 1.0 op_sel_hi:[1,0,0] neg_lo:[1,0,0] neg_hi:[1,0,0]
	v_pk_fma_f32 v[136:137], v[136:137], 2.0, 1.0 op_sel_hi:[1,0,0] neg_lo:[1,0,0] neg_hi:[1,0,0]
	v_pk_fma_f32 v[138:139], v[138:139], 2.0, 1.0 op_sel_hi:[1,0,0] neg_lo:[1,0,0] neg_hi:[1,0,0]
	v_pk_fma_f32 v[140:141], v[140:141], 2.0, 1.0 op_sel_hi:[1,0,0] neg_lo:[1,0,0] neg_hi:[1,0,0]
	v_pk_fma_f32 v[142:143], v[142:143], 2.0, 1.0 op_sel_hi:[1,0,0] neg_lo:[1,0,0] neg_hi:[1,0,0]
	v_pk_fma_f32 v[144:145], v[144:145], 2.0, 1.0 op_sel_hi:[1,0,0] neg_lo:[1,0,0] neg_hi:[1,0,0]
	v_cvt_pk_f16_f32 v146, v130, v131
	v_cvt_pk_f16_f32 v147, v132, v133
	v_cvt_pk_f16_f32 v148, v134, v135
	v_cvt_pk_f16_f32 v149, v136, v137
	v_cvt_pk_f16_f32 v150, v138, v139
	v_cvt_pk_f16_f32 v151, v140, v141
	v_cvt_pk_f16_f32 v152, v142, v143
	v_cvt_pk_f16_f32 v153, v144, v145
	s_nop 1
	v_permlane32_swap_b32_e32 v146, v148
	v_permlane32_swap_b32_e32 v147, v149
	v_permlane32_swap_b32_e32 v150, v152
	v_permlane32_swap_b32_e32 v151, v153
	global_store_dwordx4 v157, v[146:149], s[32:33] sc1
	global_store_dwordx4 v157, v[150:153], s[32:33] offset:1024 sc1
	s_add_u32 s32, s32, 0x10000
	s_addc_u32 s33, s33, 0
	s_waitcnt lgkmcnt(4)
	v_mfma_f32_32x32x16_f16 v[98:113], v[82:85], v[34:37], 0
	v_mfma_f32_32x32x16_f16 v[98:113], v[86:89], v[38:41], v[98:113]
	v_mfma_f32_32x32x16_f16 v[98:113], v[90:93], v[42:45], v[98:113]
	v_mfma_f32_32x32x16_f16 v[98:113], v[94:97], v[46:49], v[98:113]
	v_pk_fma_f32 v[130:131], v[114:115], s[4:5], v[66:67] op_sel_hi:[1,0,1]
	v_pk_fma_f32 v[132:133], v[116:117], s[4:5], v[68:69] op_sel_hi:[1,0,1]
	v_pk_fma_f32 v[134:135], v[118:119], s[4:5], v[70:71] op_sel_hi:[1,0,1]
	v_pk_fma_f32 v[136:137], v[120:121], s[4:5], v[72:73] op_sel_hi:[1,0,1]
	v_pk_fma_f32 v[138:139], v[122:123], s[4:5], v[74:75] op_sel_hi:[1,0,1]
	v_pk_fma_f32 v[140:141], v[124:125], s[4:5], v[76:77] op_sel_hi:[1,0,1]
	v_pk_fma_f32 v[142:143], v[126:127], s[4:5], v[78:79] op_sel_hi:[1,0,1]
	v_pk_fma_f32 v[144:145], v[128:129], s[4:5], v[80:81] op_sel_hi:[1,0,1]
	v_exp_f32_e32 v130, v130
	v_exp_f32_e32 v131, v131
	v_exp_f32_e32 v132, v132
	v_exp_f32_e32 v133, v133
	v_exp_f32_e32 v134, v134
	v_exp_f32_e32 v135, v135
	v_exp_f32_e32 v136, v136
	v_exp_f32_e32 v137, v137
	v_exp_f32_e32 v138, v138
	v_exp_f32_e32 v139, v139
	v_exp_f32_e32 v140, v140
	v_exp_f32_e32 v141, v141
	v_exp_f32_e32 v142, v142
	v_exp_f32_e32 v143, v143
	v_exp_f32_e32 v144, v144
	v_exp_f32_e32 v145, v145
	v_pk_add_f32 v[130:131], v[130:131], 1.0 op_sel_hi:[1,0]
	v_pk_add_f32 v[132:133], v[132:133], 1.0 op_sel_hi:[1,0]
	v_pk_add_f32 v[134:135], v[134:135], 1.0 op_sel_hi:[1,0]
	v_pk_add_f32 v[136:137], v[136:137], 1.0 op_sel_hi:[1,0]
	v_pk_add_f32 v[138:139], v[138:139], 1.0 op_sel_hi:[1,0]
	v_pk_add_f32 v[140:141], v[140:141], 1.0 op_sel_hi:[1,0]
	v_pk_add_f32 v[142:143], v[142:143], 1.0 op_sel_hi:[1,0]
	v_pk_add_f32 v[144:145], v[144:145], 1.0 op_sel_hi:[1,0]
	v_rcp_f32_e32 v130, v130
	v_rcp_f32_e32 v131, v131
	v_rcp_f32_e32 v132, v132
	v_rcp_f32_e32 v133, v133
	v_rcp_f32_e32 v134, v134
	v_rcp_f32_e32 v135, v135
	v_rcp_f32_e32 v136, v136
	v_rcp_f32_e32 v137, v137
	v_rcp_f32_e32 v138, v138
	v_rcp_f32_e32 v139, v139
	v_rcp_f32_e32 v140, v140
	v_rcp_f32_e32 v141, v141
	v_rcp_f32_e32 v142, v142
	v_rcp_f32_e32 v143, v143
	v_rcp_f32_e32 v144, v144
	v_rcp_f32_e32 v145, v145
	v_pk_fma_f32 v[130:131], v[130:131], 2.0, 1.0 op_sel_hi:[1,0,0] neg_lo:[1,0,0] neg_hi:[1,0,0]
	v_pk_fma_f32 v[132:133], v[132:133], 2.0, 1.0 op_sel_hi:[1,0,0] neg_lo:[1,0,0] neg_hi:[1,0,0]
	v_pk_fma_f32 v[134:135], v[134:135], 2.0, 1.0 op_sel_hi:[1,0,0] neg_lo:[1,0,0] neg_hi:[1,0,0]
	v_pk_fma_f32 v[136:137], v[136:137], 2.0, 1.0 op_sel_hi:[1,0,0] neg_lo:[1,0,0] neg_hi:[1,0,0]
	v_pk_fma_f32 v[138:139], v[138:139], 2.0, 1.0 op_sel_hi:[1,0,0] neg_lo:[1,0,0] neg_hi:[1,0,0]
	v_pk_fma_f32 v[140:141], v[140:141], 2.0, 1.0 op_sel_hi:[1,0,0] neg_lo:[1,0,0] neg_hi:[1,0,0]
	v_pk_fma_f32 v[142:143], v[142:143], 2.0, 1.0 op_sel_hi:[1,0,0] neg_lo:[1,0,0] neg_hi:[1,0,0]
	v_pk_fma_f32 v[144:145], v[144:145], 2.0, 1.0 op_sel_hi:[1,0,0] neg_lo:[1,0,0] neg_hi:[1,0,0]
	v_cvt_pk_f16_f32 v146, v130, v131
	v_cvt_pk_f16_f32 v147, v132, v133
	v_cvt_pk_f16_f32 v148, v134, v135
	v_cvt_pk_f16_f32 v149, v136, v137
	v_cvt_pk_f16_f32 v150, v138, v139
	v_cvt_pk_f16_f32 v151, v140, v141
	v_cvt_pk_f16_f32 v152, v142, v143
	v_cvt_pk_f16_f32 v153, v144, v145
	s_nop 1
	v_permlane32_swap_b32_e32 v146, v148
	v_permlane32_swap_b32_e32 v147, v149
	v_permlane32_swap_b32_e32 v150, v152
	v_permlane32_swap_b32_e32 v151, v153
	global_store_dwordx4 v157, v[146:149], s[32:33] sc1
	global_store_dwordx4 v157, v[150:153], s[32:33] offset:1024 sc1
	s_add_u32 s32, s32, 0x10000
	s_addc_u32 s33, s33, 0
	s_waitcnt lgkmcnt(0)
	v_mfma_f32_32x32x16_f16 v[114:129], v[82:85], v[50:53], 0
	v_mfma_f32_32x32x16_f16 v[114:129], v[86:89], v[54:57], v[114:129]
	v_mfma_f32_32x32x16_f16 v[114:129], v[90:93], v[58:61], v[114:129]
	v_mfma_f32_32x32x16_f16 v[114:129], v[94:97], v[62:65], v[114:129]
	v_pk_fma_f32 v[130:131], v[98:99], s[4:5], v[66:67] op_sel_hi:[1,0,1]
	v_pk_fma_f32 v[132:133], v[100:101], s[4:5], v[68:69] op_sel_hi:[1,0,1]
	v_pk_fma_f32 v[134:135], v[102:103], s[4:5], v[70:71] op_sel_hi:[1,0,1]
	v_pk_fma_f32 v[136:137], v[104:105], s[4:5], v[72:73] op_sel_hi:[1,0,1]
	v_pk_fma_f32 v[138:139], v[106:107], s[4:5], v[74:75] op_sel_hi:[1,0,1]
	v_pk_fma_f32 v[140:141], v[108:109], s[4:5], v[76:77] op_sel_hi:[1,0,1]
	v_pk_fma_f32 v[142:143], v[110:111], s[4:5], v[78:79] op_sel_hi:[1,0,1]
	v_pk_fma_f32 v[144:145], v[112:113], s[4:5], v[80:81] op_sel_hi:[1,0,1]
	v_exp_f32_e32 v130, v130
	v_exp_f32_e32 v131, v131
	v_exp_f32_e32 v132, v132
	v_exp_f32_e32 v133, v133
	v_exp_f32_e32 v134, v134
	v_exp_f32_e32 v135, v135
	v_exp_f32_e32 v136, v136
	v_exp_f32_e32 v137, v137
	v_exp_f32_e32 v138, v138
	v_exp_f32_e32 v139, v139
	v_exp_f32_e32 v140, v140
	v_exp_f32_e32 v141, v141
	v_exp_f32_e32 v142, v142
	v_exp_f32_e32 v143, v143
	v_exp_f32_e32 v144, v144
	v_exp_f32_e32 v145, v145
	v_pk_add_f32 v[130:131], v[130:131], 1.0 op_sel_hi:[1,0]
	v_pk_add_f32 v[132:133], v[132:133], 1.0 op_sel_hi:[1,0]
	v_pk_add_f32 v[134:135], v[134:135], 1.0 op_sel_hi:[1,0]
	v_pk_add_f32 v[136:137], v[136:137], 1.0 op_sel_hi:[1,0]
	v_pk_add_f32 v[138:139], v[138:139], 1.0 op_sel_hi:[1,0]
	v_pk_add_f32 v[140:141], v[140:141], 1.0 op_sel_hi:[1,0]
	v_pk_add_f32 v[142:143], v[142:143], 1.0 op_sel_hi:[1,0]
	v_pk_add_f32 v[144:145], v[144:145], 1.0 op_sel_hi:[1,0]
	v_rcp_f32_e32 v130, v130
	v_rcp_f32_e32 v131, v131
	v_rcp_f32_e32 v132, v132
	v_rcp_f32_e32 v133, v133
	v_rcp_f32_e32 v134, v134
	v_rcp_f32_e32 v135, v135
	v_rcp_f32_e32 v136, v136
	v_rcp_f32_e32 v137, v137
	v_rcp_f32_e32 v138, v138
	v_rcp_f32_e32 v139, v139
	v_rcp_f32_e32 v140, v140
	v_rcp_f32_e32 v141, v141
	v_rcp_f32_e32 v142, v142
	v_rcp_f32_e32 v143, v143
	v_rcp_f32_e32 v144, v144
	v_rcp_f32_e32 v145, v145
	v_pk_fma_f32 v[130:131], v[130:131], 2.0, 1.0 op_sel_hi:[1,0,0] neg_lo:[1,0,0] neg_hi:[1,0,0]
	v_pk_fma_f32 v[132:133], v[132:133], 2.0, 1.0 op_sel_hi:[1,0,0] neg_lo:[1,0,0] neg_hi:[1,0,0]
	v_pk_fma_f32 v[134:135], v[134:135], 2.0, 1.0 op_sel_hi:[1,0,0] neg_lo:[1,0,0] neg_hi:[1,0,0]
	v_pk_fma_f32 v[136:137], v[136:137], 2.0, 1.0 op_sel_hi:[1,0,0] neg_lo:[1,0,0] neg_hi:[1,0,0]
	v_pk_fma_f32 v[138:139], v[138:139], 2.0, 1.0 op_sel_hi:[1,0,0] neg_lo:[1,0,0] neg_hi:[1,0,0]
	v_pk_fma_f32 v[140:141], v[140:141], 2.0, 1.0 op_sel_hi:[1,0,0] neg_lo:[1,0,0] neg_hi:[1,0,0]
	v_pk_fma_f32 v[142:143], v[142:143], 2.0, 1.0 op_sel_hi:[1,0,0] neg_lo:[1,0,0] neg_hi:[1,0,0]
	v_pk_fma_f32 v[144:145], v[144:145], 2.0, 1.0 op_sel_hi:[1,0,0] neg_lo:[1,0,0] neg_hi:[1,0,0]
	v_cvt_pk_f16_f32 v146, v130, v131
	v_cvt_pk_f16_f32 v147, v132, v133
	v_cvt_pk_f16_f32 v148, v134, v135
	v_cvt_pk_f16_f32 v149, v136, v137
	v_cvt_pk_f16_f32 v150, v138, v139
	v_cvt_pk_f16_f32 v151, v140, v141
	v_cvt_pk_f16_f32 v152, v142, v143
	v_cvt_pk_f16_f32 v153, v144, v145
	s_nop 1
	v_permlane32_swap_b32_e32 v146, v148
	v_permlane32_swap_b32_e32 v147, v149
	v_permlane32_swap_b32_e32 v150, v152
	v_permlane32_swap_b32_e32 v151, v153
	global_store_dwordx4 v157, v[146:149], s[32:33] sc1
	global_store_dwordx4 v157, v[150:153], s[32:33] offset:1024 sc1
	s_add_u32 s32, s32, 0x10000
	s_addc_u32 s33, s33, 0
	s_nop 7
	v_pk_fma_f32 v[130:131], v[114:115], s[4:5], v[66:67] op_sel_hi:[1,0,1]
	v_pk_fma_f32 v[132:133], v[116:117], s[4:5], v[68:69] op_sel_hi:[1,0,1]
	v_pk_fma_f32 v[134:135], v[118:119], s[4:5], v[70:71] op_sel_hi:[1,0,1]
	v_pk_fma_f32 v[136:137], v[120:121], s[4:5], v[72:73] op_sel_hi:[1,0,1]
	v_pk_fma_f32 v[138:139], v[122:123], s[4:5], v[74:75] op_sel_hi:[1,0,1]
	v_pk_fma_f32 v[140:141], v[124:125], s[4:5], v[76:77] op_sel_hi:[1,0,1]
	v_pk_fma_f32 v[142:143], v[126:127], s[4:5], v[78:79] op_sel_hi:[1,0,1]
	v_pk_fma_f32 v[144:145], v[128:129], s[4:5], v[80:81] op_sel_hi:[1,0,1]
	v_exp_f32_e32 v130, v130
	v_exp_f32_e32 v131, v131
	v_exp_f32_e32 v132, v132
	v_exp_f32_e32 v133, v133
	v_exp_f32_e32 v134, v134
	v_exp_f32_e32 v135, v135
	v_exp_f32_e32 v136, v136
	v_exp_f32_e32 v137, v137
	v_exp_f32_e32 v138, v138
	v_exp_f32_e32 v139, v139
	v_exp_f32_e32 v140, v140
	v_exp_f32_e32 v141, v141
	v_exp_f32_e32 v142, v142
	v_exp_f32_e32 v143, v143
	v_exp_f32_e32 v144, v144
	v_exp_f32_e32 v145, v145
	v_pk_add_f32 v[130:131], v[130:131], 1.0 op_sel_hi:[1,0]
	v_pk_add_f32 v[132:133], v[132:133], 1.0 op_sel_hi:[1,0]
	v_pk_add_f32 v[134:135], v[134:135], 1.0 op_sel_hi:[1,0]
	v_pk_add_f32 v[136:137], v[136:137], 1.0 op_sel_hi:[1,0]
	v_pk_add_f32 v[138:139], v[138:139], 1.0 op_sel_hi:[1,0]
	v_pk_add_f32 v[140:141], v[140:141], 1.0 op_sel_hi:[1,0]
	v_pk_add_f32 v[142:143], v[142:143], 1.0 op_sel_hi:[1,0]
	v_pk_add_f32 v[144:145], v[144:145], 1.0 op_sel_hi:[1,0]
	v_rcp_f32_e32 v130, v130
	v_rcp_f32_e32 v131, v131
	v_rcp_f32_e32 v132, v132
	v_rcp_f32_e32 v133, v133
	v_rcp_f32_e32 v134, v134
	v_rcp_f32_e32 v135, v135
	v_rcp_f32_e32 v136, v136
	v_rcp_f32_e32 v137, v137
	v_rcp_f32_e32 v138, v138
	v_rcp_f32_e32 v139, v139
	v_rcp_f32_e32 v140, v140
	v_rcp_f32_e32 v141, v141
	v_rcp_f32_e32 v142, v142
	v_rcp_f32_e32 v143, v143
	v_rcp_f32_e32 v144, v144
	v_rcp_f32_e32 v145, v145
	v_pk_fma_f32 v[130:131], v[130:131], 2.0, 1.0 op_sel_hi:[1,0,0] neg_lo:[1,0,0] neg_hi:[1,0,0]
	v_pk_fma_f32 v[132:133], v[132:133], 2.0, 1.0 op_sel_hi:[1,0,0] neg_lo:[1,0,0] neg_hi:[1,0,0]
	v_pk_fma_f32 v[134:135], v[134:135], 2.0, 1.0 op_sel_hi:[1,0,0] neg_lo:[1,0,0] neg_hi:[1,0,0]
	v_pk_fma_f32 v[136:137], v[136:137], 2.0, 1.0 op_sel_hi:[1,0,0] neg_lo:[1,0,0] neg_hi:[1,0,0]
	v_pk_fma_f32 v[138:139], v[138:139], 2.0, 1.0 op_sel_hi:[1,0,0] neg_lo:[1,0,0] neg_hi:[1,0,0]
	v_pk_fma_f32 v[140:141], v[140:141], 2.0, 1.0 op_sel_hi:[1,0,0] neg_lo:[1,0,0] neg_hi:[1,0,0]
	v_pk_fma_f32 v[142:143], v[142:143], 2.0, 1.0 op_sel_hi:[1,0,0] neg_lo:[1,0,0] neg_hi:[1,0,0]
	v_pk_fma_f32 v[144:145], v[144:145], 2.0, 1.0 op_sel_hi:[1,0,0] neg_lo:[1,0,0] neg_hi:[1,0,0]
	v_cvt_pk_f16_f32 v146, v130, v131
	v_cvt_pk_f16_f32 v147, v132, v133
	v_cvt_pk_f16_f32 v148, v134, v135
	v_cvt_pk_f16_f32 v149, v136, v137
	v_cvt_pk_f16_f32 v150, v138, v139
	v_cvt_pk_f16_f32 v151, v140, v141
	v_cvt_pk_f16_f32 v152, v142, v143
	v_cvt_pk_f16_f32 v153, v144, v145
	s_nop 1
	v_permlane32_swap_b32_e32 v146, v148
	v_permlane32_swap_b32_e32 v147, v149
	v_permlane32_swap_b32_e32 v150, v152
	v_permlane32_swap_b32_e32 v151, v153
	global_store_dwordx4 v157, v[146:149], s[32:33] sc1
	global_store_dwordx4 v157, v[150:153], s[32:33] offset:1024 sc1
	s_endpgm
